# kernel entry: every workgroup touches a 30-line slice of the kernel's own code (s_getpc base) so the later phases' instructions are in L2 / the memory-side cache instead of cold HBM
# speedup vs baseline: 1.0064x; 1.0064x over previous
_Z8mega_fwd4Args:
	s_getpc_b64 s[98:99]
	s_and_b32 s98, s98, 0xffffff00
	s_lshr_b32 s97, s2, 3
	s_mul_i32 s97, s97, 0xf00
	s_add_u32 s98, s98, s97
	s_addc_u32 s99, s99, 0
	v_min_u32_e32 v253, 29, v0
	v_lshlrev_b32_e32 v253, 7, v253
	global_load_dword v254, v253, s[98:99]
	s_load_dwordx4 s[88:91], s[0:1], 0x80
	s_load_dword s84, s[0:1], 0x90
	s_add_u32 s4, s0, 0x90
	s_addc_u32 s5, s1, 0
	v_readfirstlane_b32 s10, v0
	v_writelane_b32 v252, s4, 0
	s_waitcnt lgkmcnt(0)
	s_and_b32 s3, s84, 7
	s_mov_b32 s33, s2
	s_cmp_lg_u32 s3, 0
	s_mov_b32 s8, s2
	v_writelane_b32 v252, s5, 1
	s_cbranch_scc1 .LBB0_2
	s_ashr_i32 s4, s2, 31
	s_lshr_b32 s4, s4, 29
	s_add_i32 s4, s2, s4
	s_and_b32 s5, s4, -8
	s_ashr_i32 s3, s84, 3
	s_sub_i32 s5, s2, s5
	s_mul_i32 s3, s3, s5
	s_ashr_i32 s4, s4, 3
	s_add_i32 s8, s3, s4

	.amdhsa_kernel _Z8mega_fwd4Args
		.amdhsa_group_segment_fixed_size 0
		.amdhsa_private_segment_fixed_size 0
		.amdhsa_kernarg_size 400
		.amdhsa_user_sgpr_count 2
		.amdhsa_user_sgpr_dispatch_ptr 0
		.amdhsa_user_sgpr_queue_ptr 0
		.amdhsa_user_sgpr_kernarg_segment_ptr 1
		.amdhsa_user_sgpr_dispatch_id 0
		.amdhsa_user_sgpr_kernarg_preload_length 0
		.amdhsa_user_sgpr_kernarg_preload_offset 0
		.amdhsa_user_sgpr_private_segment_size 0
		.amdhsa_uses_dynamic_stack 0
		.amdhsa_enable_private_segment 0
		.amdhsa_system_sgpr_workgroup_id_x 1
		.amdhsa_system_sgpr_workgroup_id_y 0
		.amdhsa_system_sgpr_workgroup_id_z 0
		.amdhsa_system_sgpr_workgroup_info 0
		.amdhsa_system_vgpr_workitem_id 0
		.amdhsa_next_free_vgpr 255
		.amdhsa_next_free_sgpr 100
		.amdhsa_accum_offset 256
		.amdhsa_reserve_vcc 1
		.amdhsa_float_round_mode_32 0
		.amdhsa_float_round_mode_16_64 0
		.amdhsa_float_denorm_mode_32 3
		.amdhsa_float_denorm_mode_16_64 3
		.amdhsa_dx10_clamp 1
		.amdhsa_ieee_mode 1
		.amdhsa_fp16_overflow 0
		.amdhsa_tg_split 0
		.amdhsa_exception_fp_ieee_invalid_op 0
		.amdhsa_exception_fp_denorm_src 0
		.amdhsa_exception_fp_ieee_div_zero 0
		.amdhsa_exception_fp_ieee_overflow 0
		.amdhsa_exception_fp_ieee_underflow 0
		.amdhsa_exception_fp_ieee_inexact 0
		.amdhsa_exception_int_div_zero 0
	.end_amdhsa_kernel

amdhsa.kernels:
  - .agpr_count:     0
    .args:
      - .offset:         0
        .size:           144
        .value_kind:     by_value
      - .offset:         144
        .size:           4
        .value_kind:     hidden_block_count_x
      - .offset:         148
        .size:           4
        .value_kind:     hidden_block_count_y
      - .offset:         152
        .size:           4
        .value_kind:     hidden_block_count_z
      - .offset:         156
        .size:           2
        .value_kind:     hidden_group_size_x
      - .offset:         158
        .size:           2
        .value_kind:     hidden_group_size_y
      - .offset:         160
        .size:           2
        .value_kind:     hidden_group_size_z
      - .offset:         162
        .size:           2
        .value_kind:     hidden_remainder_x
      - .offset:         164
        .size:           2
        .value_kind:     hidden_remainder_y
      - .offset:         166
        .size:           2
        .value_kind:     hidden_remainder_z
      - .offset:         184
        .size:           8
        .value_kind:     hidden_global_offset_x
      - .offset:         192
        .size:           8
        .value_kind:     hidden_global_offset_y
      - .offset:         200
        .size:           8
        .value_kind:     hidden_global_offset_z
      - .offset:         208
        .size:           2
        .value_kind:     hidden_grid_dims
      - .offset:         264
        .size:           4
        .value_kind:     hidden_dynamic_lds_size
    .group_segment_fixed_size: 0
    .kernarg_segment_align: 8
    .kernarg_segment_size: 400
    .language:       OpenCL C
    .language_version:
      - 2
      - 0
    .max_flat_workgroup_size: 512
    .name:           _Z8mega_fwd4Args
    .private_segment_fixed_size: 0
    .sgpr_count:     106
    .sgpr_spill_count: 43
    .symbol:         _Z8mega_fwd4Args.kd
    .uniform_work_group_size: 1
    .uses_dynamic_stack: false
    .vgpr_count:     255
    .vgpr_spill_count: 0
    .wavefront_size: 64
